# k_bucketsort: waves with a >64-entry run stay on the rank-based fast path (tail entries held in spare VGPRs) instead of the serialized slow path
# speedup vs baseline: 1.0817x; 1.0097x over previous
.LBB2_48:
	s_or_b64 exec, exec, s[60:61]
	s_and_b64 s[48:49], s[48:49], s[0:1]
	s_cmpk_gt_i32 s33, 0x3000
	s_cbranch_scc1 .Lbs_cnt_slow
	s_mov_b32 s71, 0
	s_cmp_eq_u64 s[44:45], -1
	s_cselect_b32 s70, 0x1, 0
	s_or_b32 s71, s71, s70
	s_cmp_eq_u64 s[42:43], -1
	s_cselect_b32 s70, 0x2, 0
	s_or_b32 s71, s71, s70
	s_cmp_eq_u64 s[40:41], -1
	s_cselect_b32 s70, 0x4, 0
	s_or_b32 s71, s71, s70
	s_cmp_eq_u64 s[38:39], -1
	s_cselect_b32 s70, 0x8, 0
	s_or_b32 s71, s71, s70
	s_cmp_eq_u64 s[36:37], -1
	s_cselect_b32 s70, 0x10, 0
	s_or_b32 s71, s71, s70
	s_cmp_eq_u64 s[34:35], -1
	s_cselect_b32 s70, 0x20, 0
	s_or_b32 s71, s71, s70
	s_cmp_eq_u64 s[30:31], -1
	s_cselect_b32 s70, 0x40, 0
	s_or_b32 s71, s71, s70
	s_cmp_eq_u64 s[28:29], -1
	s_cselect_b32 s70, 0x80, 0
	s_or_b32 s71, s71, s70
	s_cmp_eq_u64 s[26:27], -1
	s_cselect_b32 s70, 0x100, 0
	s_or_b32 s71, s71, s70
	s_cmp_eq_u64 s[24:25], -1
	s_cselect_b32 s70, 0x200, 0
	s_or_b32 s71, s71, s70
	s_cmp_eq_u64 s[22:23], -1
	s_cselect_b32 s70, 0x400, 0
	s_or_b32 s71, s71, s70
	s_cmp_eq_u64 s[20:21], -1
	s_cselect_b32 s70, 0x800, 0
	s_or_b32 s71, s71, s70
	s_cmp_eq_u64 s[18:19], -1
	s_cselect_b32 s70, 0x1000, 0
	s_or_b32 s71, s71, s70
	s_cmp_eq_u64 s[48:49], -1
	s_cselect_b32 s70, 0x2000, 0
	s_or_b32 s71, s71, s70
	s_mov_b64 s[60:61], s[18:19]
	s_mov_b64 s[78:79], 0
	s_mov_b64 s[80:81], 0
	s_mov_b64 s[6:7], exec
	s_cmp_eq_u32 s71, 0
	s_cbranch_scc1 .Lbs_fast_go
	s_ff1_i32_b32 s72, s71
	s_bitset0_b32 s71, s72
	s_lshl_b32 s73, s72, 6
	v_add_u32_e32 v58, s73, v9
	ds_read_b32 v57, v58
	v_add_u32_e32 v58, s73, v8
	ds_read_b32 v56, v58 offset:52224
	v_or_b32_e32 v58, 64, v2
	s_waitcnt lgkmcnt(0)
	v_readfirstlane_b32 s74, v57
	s_cmpk_gt_i32 s74, 0x80
	s_cbranch_scc1 .Lbs_cnt_slow_w
	v_cmp_lt_u32_e64 s[78:79], v58, v57
	v_add_u32_e32 v56, v56, v2
	v_lshlrev_b32_e32 v58, 10, v0
	v_and_b32_e32 v58, 0xf0000, v58
	s_lshl_b32 s73, s72, 20
	v_lshl_add_u32 v56, v56, 2, v58
	v_add_u32_e32 v58, s73, v56
	v_lshrrev_b32_e32 v57, 1, v58
	s_and_b64 exec, s[6:7], s[78:79]
	global_load_dword v56, v58, s[56:57] offset:256 nt
	global_load_ushort v57, v57, s[58:59] offset:128 nt
	s_mov_b64 exec, s[6:7]
	s_cmp_eq_u32 s71, 0
	s_cbranch_scc1 .Lbs_fast_go
	s_ff1_i32_b32 s72, s71
	s_bitset0_b32 s71, s72
	s_cmp_lg_u32 s71, 0
	s_cbranch_scc1 .Lbs_cnt_slow_w
	s_lshl_b32 s73, s72, 6
	v_add_u32_e32 v61, s73, v9
	ds_read_b32 v60, v61
	v_add_u32_e32 v61, s73, v8
	ds_read_b32 v59, v61 offset:52224
	v_or_b32_e32 v61, 64, v2
	s_waitcnt lgkmcnt(0)
	v_readfirstlane_b32 s74, v60
	s_cmpk_gt_i32 s74, 0x80
	s_cbranch_scc1 .Lbs_cnt_slow_w
	v_cmp_lt_u32_e64 s[80:81], v61, v60
	v_add_u32_e32 v59, v59, v2
	v_lshlrev_b32_e32 v61, 10, v0
	v_and_b32_e32 v61, 0xf0000, v61
	s_lshl_b32 s73, s72, 20
	v_lshl_add_u32 v59, v59, 2, v61
	v_add_u32_e32 v61, s73, v59
	v_lshrrev_b32_e32 v60, 1, v61
	s_and_b64 exec, s[6:7], s[80:81]
	global_load_dword v59, v61, s[56:57] offset:256 nt
	global_load_ushort v60, v60, s[58:59] offset:128 nt
	s_mov_b64 exec, s[6:7]
.Lbs_fast_go:
	s_waitcnt vmcnt(0)
	v_mov_b32_e32 v62, 1
	s_mov_b32 s62, 0x1ffff
	s_mov_b64 s[6:7], exec
	s_and_b64 exec, s[6:7], s[44:45]
	v_lshrrev_b32_e32 v54, 15, v46
	v_lshlrev_b32_e32 v47, 17, v47
	v_and_b32_e32 v54, 0x1fffc, v54
	v_and_or_b32 v46, v46, s62, v47
	ds_add_rtn_u32 v47, v54, v62 offset:49152
	s_and_b64 exec, s[6:7], s[42:43]
	v_lshrrev_b32_e32 v53, 15, v41
	v_lshlrev_b32_e32 v39, 17, v39
	v_and_b32_e32 v53, 0x1fffc, v53
	v_and_or_b32 v41, v41, s62, v39
	ds_add_rtn_u32 v39, v53, v62 offset:49152
	s_and_b64 exec, s[6:7], s[40:41]
	v_lshrrev_b32_e32 v52, 15, v36
	v_lshlrev_b32_e32 v37, 17, v37
	v_and_b32_e32 v52, 0x1fffc, v52
	v_and_or_b32 v36, v36, s62, v37
	ds_add_rtn_u32 v37, v52, v62 offset:49152
	s_and_b64 exec, s[6:7], s[38:39]
	v_lshrrev_b32_e32 v51, 15, v34
	v_lshlrev_b32_e32 v32, 17, v32
	v_and_b32_e32 v51, 0x1fffc, v51
	v_and_or_b32 v34, v34, s62, v32
	ds_add_rtn_u32 v32, v51, v62 offset:49152
	s_and_b64 exec, s[6:7], s[36:37]
	v_lshrrev_b32_e32 v50, 15, v29
	v_lshlrev_b32_e32 v30, 17, v30
	v_and_b32_e32 v50, 0x1fffc, v50
	v_and_or_b32 v29, v29, s62, v30
	ds_add_rtn_u32 v30, v50, v62 offset:49152
	s_and_b64 exec, s[6:7], s[34:35]
	v_lshrrev_b32_e32 v49, 15, v28
	v_lshlrev_b32_e32 v27, 17, v27
	v_and_b32_e32 v49, 0x1fffc, v49
	v_and_or_b32 v28, v28, s62, v27
	ds_add_rtn_u32 v27, v49, v62 offset:49152
	s_and_b64 exec, s[6:7], s[30:31]
	v_lshrrev_b32_e32 v48, 15, v25
	v_lshlrev_b32_e32 v26, 17, v26
	v_and_b32_e32 v48, 0x1fffc, v48
	v_and_or_b32 v25, v25, s62, v26
	ds_add_rtn_u32 v26, v48, v62 offset:49152
	s_and_b64 exec, s[6:7], s[28:29]
	v_lshrrev_b32_e32 v45, 15, v24
	v_lshlrev_b32_e32 v23, 17, v23
	v_and_b32_e32 v45, 0x1fffc, v45
	v_and_or_b32 v24, v24, s62, v23
	ds_add_rtn_u32 v23, v45, v62 offset:49152
	s_and_b64 exec, s[6:7], s[26:27]
	v_lshrrev_b32_e32 v42, 15, v21
	v_lshlrev_b32_e32 v22, 17, v22
	v_and_b32_e32 v42, 0x1fffc, v42
	v_and_or_b32 v21, v21, s62, v22
	ds_add_rtn_u32 v22, v42, v62 offset:49152
	s_and_b64 exec, s[6:7], s[24:25]
	v_lshrrev_b32_e32 v38, 15, v20
	v_lshlrev_b32_e32 v19, 17, v19
	v_and_b32_e32 v38, 0x1fffc, v38
	v_and_or_b32 v20, v20, s62, v19
	ds_add_rtn_u32 v19, v38, v62 offset:49152
	s_and_b64 exec, s[6:7], s[22:23]
	v_lshrrev_b32_e32 v35, 15, v17
	v_lshlrev_b32_e32 v18, 17, v18
	v_and_b32_e32 v35, 0x1fffc, v35
	v_and_or_b32 v17, v17, s62, v18
	ds_add_rtn_u32 v18, v35, v62 offset:49152
	s_and_b64 exec, s[6:7], s[20:21]
	v_lshrrev_b32_e32 v33, 15, v16
	v_lshlrev_b32_e32 v15, 17, v15
	v_and_b32_e32 v33, 0x1fffc, v33
	v_and_or_b32 v16, v16, s62, v15
	ds_add_rtn_u32 v15, v33, v62 offset:49152
	s_and_b64 exec, s[6:7], s[60:61]
	v_lshrrev_b32_e32 v31, 15, v13
	v_lshlrev_b32_e32 v14, 17, v14
	v_and_b32_e32 v31, 0x1fffc, v31
	v_and_or_b32 v13, v13, s62, v14
	ds_add_rtn_u32 v14, v31, v62 offset:49152
	s_and_b64 exec, s[6:7], s[48:49]
	v_lshrrev_b32_e32 v55, 15, v12
	v_lshlrev_b32_e32 v11, 17, v11
	v_and_b32_e32 v55, 0x1fffc, v55
	v_and_or_b32 v12, v12, s62, v11
	ds_add_rtn_u32 v11, v55, v62 offset:49152
	s_and_b64 exec, s[6:7], s[78:79]
	v_lshrrev_b32_e32 v58, 15, v56
	v_lshlrev_b32_e32 v57, 17, v57
	v_and_b32_e32 v58, 0x1fffc, v58
	v_and_or_b32 v56, v56, s62, v57
	ds_add_rtn_u32 v57, v58, v62 offset:49152
	s_and_b64 exec, s[6:7], s[80:81]
	v_lshrrev_b32_e32 v61, 15, v59
	v_lshlrev_b32_e32 v60, 17, v60
	v_and_b32_e32 v61, 0x1fffc, v61
	v_and_or_b32 v59, v59, s62, v60
	ds_add_rtn_u32 v60, v61, v62 offset:49152
	s_mov_b64 exec, s[6:7]
	s_mov_b32 s63, 1
	s_branch .Lbs_cnt_join
.Lbs_cnt_slow_w:
	s_mov_b64 exec, s[6:7]
	s_waitcnt vmcnt(0)

.LBB2_134:
	s_or_b64 exec, exec, s[2:3]
	s_waitcnt lgkmcnt(0)
	s_barrier
	s_cmp_eq_u32 s63, 0
	s_cbranch_scc1 .Lbs_slow
	v_mov_b32_e32 v3, 0
	ds_read_b32 v3, v3 offset:54144
	s_mov_b64 s[4:5], -1
	s_mov_b64 s[6:7], 0
	s_mov_b64 s[2:3], exec
	s_waitcnt lgkmcnt(0)
	v_readfirstlane_b32 s8, v3
	s_cmp_lg_u32 s8, 0
	s_cbranch_scc1 .Lbs_pos_atomic
	s_and_b64 exec, s[2:3], s[44:45]
	ds_read_b32 v54, v54 offset:49152
	s_and_b64 exec, s[2:3], s[42:43]
	ds_read_b32 v53, v53 offset:49152
	s_and_b64 exec, s[2:3], s[40:41]
	ds_read_b32 v52, v52 offset:49152
	s_and_b64 exec, s[2:3], s[38:39]
	ds_read_b32 v51, v51 offset:49152
	s_and_b64 exec, s[2:3], s[36:37]
	ds_read_b32 v50, v50 offset:49152
	s_and_b64 exec, s[2:3], s[34:35]
	ds_read_b32 v49, v49 offset:49152
	s_and_b64 exec, s[2:3], s[30:31]
	ds_read_b32 v48, v48 offset:49152
	s_and_b64 exec, s[2:3], s[28:29]
	ds_read_b32 v45, v45 offset:49152
	s_and_b64 exec, s[2:3], s[26:27]
	ds_read_b32 v42, v42 offset:49152
	s_and_b64 exec, s[2:3], s[24:25]
	ds_read_b32 v38, v38 offset:49152
	s_and_b64 exec, s[2:3], s[22:23]
	ds_read_b32 v35, v35 offset:49152
	s_and_b64 exec, s[2:3], s[20:21]
	ds_read_b32 v33, v33 offset:49152
	s_and_b64 exec, s[2:3], s[60:61]
	ds_read_b32 v31, v31 offset:49152
	s_and_b64 exec, s[2:3], s[48:49]
	ds_read_b32 v55, v55 offset:49152
	s_and_b64 exec, s[2:3], s[78:79]
	ds_read_b32 v58, v58 offset:49152
	s_and_b64 exec, s[2:3], s[80:81]
	ds_read_b32 v61, v61 offset:49152
	s_mov_b64 exec, s[2:3]
	s_waitcnt lgkmcnt(0)
	s_and_b64 exec, s[2:3], s[44:45]
	v_add_lshl_u32 v54, v54, v47, 2
	ds_write_b32 v54, v46
	s_and_b64 exec, s[2:3], s[42:43]
	v_add_lshl_u32 v53, v53, v39, 2
	ds_write_b32 v53, v41
	s_and_b64 exec, s[2:3], s[40:41]
	v_add_lshl_u32 v52, v52, v37, 2
	ds_write_b32 v52, v36
	s_and_b64 exec, s[2:3], s[38:39]
	v_add_lshl_u32 v51, v51, v32, 2
	ds_write_b32 v51, v34
	s_and_b64 exec, s[2:3], s[36:37]
	v_add_lshl_u32 v50, v50, v30, 2
	ds_write_b32 v50, v29
	s_and_b64 exec, s[2:3], s[34:35]
	v_add_lshl_u32 v49, v49, v27, 2
	ds_write_b32 v49, v28
	s_and_b64 exec, s[2:3], s[30:31]
	v_add_lshl_u32 v48, v48, v26, 2
	ds_write_b32 v48, v25
	s_and_b64 exec, s[2:3], s[28:29]
	v_add_lshl_u32 v45, v45, v23, 2
	ds_write_b32 v45, v24
	s_and_b64 exec, s[2:3], s[26:27]
	v_add_lshl_u32 v42, v42, v22, 2
	ds_write_b32 v42, v21
	s_and_b64 exec, s[2:3], s[24:25]
	v_add_lshl_u32 v38, v38, v19, 2
	ds_write_b32 v38, v20
	s_and_b64 exec, s[2:3], s[22:23]
	v_add_lshl_u32 v35, v35, v18, 2
	ds_write_b32 v35, v17
	s_and_b64 exec, s[2:3], s[20:21]
	v_add_lshl_u32 v33, v33, v15, 2
	ds_write_b32 v33, v16
	s_and_b64 exec, s[2:3], s[60:61]
	v_add_lshl_u32 v31, v31, v14, 2
	ds_write_b32 v31, v13
	s_and_b64 exec, s[2:3], s[48:49]
	v_add_lshl_u32 v55, v55, v11, 2
	ds_write_b32 v55, v12
	s_and_b64 exec, s[2:3], s[78:79]
	v_add_lshl_u32 v58, v58, v57, 2
	ds_write_b32 v58, v56
	s_and_b64 exec, s[2:3], s[80:81]
	v_add_lshl_u32 v61, v61, v60, 2
	ds_write_b32 v61, v59
	s_mov_b64 exec, s[2:3]
	s_branch .LBB2_317
.Lbs_pos_atomic:
	s_and_b64 exec, s[2:3], s[44:45]
	ds_add_rtn_u32 v47, v54, v62 offset:49152
	s_and_b64 exec, s[2:3], s[42:43]
	ds_add_rtn_u32 v39, v53, v62 offset:49152
	s_and_b64 exec, s[2:3], s[40:41]
	ds_add_rtn_u32 v37, v52, v62 offset:49152
	s_and_b64 exec, s[2:3], s[38:39]
	ds_add_rtn_u32 v32, v51, v62 offset:49152
	s_and_b64 exec, s[2:3], s[36:37]
	ds_add_rtn_u32 v30, v50, v62 offset:49152
	s_and_b64 exec, s[2:3], s[34:35]
	ds_add_rtn_u32 v27, v49, v62 offset:49152
	s_and_b64 exec, s[2:3], s[30:31]
	ds_add_rtn_u32 v26, v48, v62 offset:49152
	s_and_b64 exec, s[2:3], s[28:29]
	ds_add_rtn_u32 v23, v45, v62 offset:49152
	s_and_b64 exec, s[2:3], s[26:27]
	ds_add_rtn_u32 v22, v42, v62 offset:49152
	s_and_b64 exec, s[2:3], s[24:25]
	ds_add_rtn_u32 v19, v38, v62 offset:49152
	s_and_b64 exec, s[2:3], s[22:23]
	ds_add_rtn_u32 v18, v35, v62 offset:49152
	s_and_b64 exec, s[2:3], s[20:21]
	ds_add_rtn_u32 v15, v33, v62 offset:49152
	s_and_b64 exec, s[2:3], s[60:61]
	ds_add_rtn_u32 v14, v31, v62 offset:49152
	s_and_b64 exec, s[2:3], s[48:49]
	ds_add_rtn_u32 v11, v55, v62 offset:49152
	s_and_b64 exec, s[2:3], s[78:79]
	ds_add_rtn_u32 v57, v58, v62 offset:49152
	s_and_b64 exec, s[2:3], s[80:81]
	ds_add_rtn_u32 v60, v61, v62 offset:49152
	s_mov_b64 exec, s[2:3]
	s_waitcnt lgkmcnt(0)
	s_and_b64 exec, s[2:3], s[44:45]
	v_lshlrev_b32_e32 v47, 2, v47
	ds_write_b32 v47, v46
	s_and_b64 exec, s[2:3], s[42:43]
	v_lshlrev_b32_e32 v39, 2, v39
	ds_write_b32 v39, v41
	s_and_b64 exec, s[2:3], s[40:41]
	v_lshlrev_b32_e32 v37, 2, v37
	ds_write_b32 v37, v36
	s_and_b64 exec, s[2:3], s[38:39]
	v_lshlrev_b32_e32 v32, 2, v32
	ds_write_b32 v32, v34
	s_and_b64 exec, s[2:3], s[36:37]
	v_lshlrev_b32_e32 v30, 2, v30
	ds_write_b32 v30, v29
	s_and_b64 exec, s[2:3], s[34:35]
	v_lshlrev_b32_e32 v27, 2, v27
	ds_write_b32 v27, v28
	s_and_b64 exec, s[2:3], s[30:31]
	v_lshlrev_b32_e32 v26, 2, v26
	ds_write_b32 v26, v25
	s_and_b64 exec, s[2:3], s[28:29]
	v_lshlrev_b32_e32 v23, 2, v23
	ds_write_b32 v23, v24
	s_and_b64 exec, s[2:3], s[26:27]
	v_lshlrev_b32_e32 v22, 2, v22
	ds_write_b32 v22, v21
	s_and_b64 exec, s[2:3], s[24:25]
	v_lshlrev_b32_e32 v19, 2, v19
	ds_write_b32 v19, v20
	s_and_b64 exec, s[2:3], s[22:23]
	v_lshlrev_b32_e32 v18, 2, v18
	ds_write_b32 v18, v17
	s_and_b64 exec, s[2:3], s[20:21]
	v_lshlrev_b32_e32 v15, 2, v15
	ds_write_b32 v15, v16
	s_and_b64 exec, s[2:3], s[60:61]
	v_lshlrev_b32_e32 v14, 2, v14
	ds_write_b32 v14, v13
	s_and_b64 exec, s[2:3], s[48:49]
	v_lshlrev_b32_e32 v11, 2, v11
	ds_write_b32 v11, v12
	s_and_b64 exec, s[2:3], s[78:79]
	v_lshlrev_b32_e32 v57, 2, v57
	ds_write_b32 v57, v56
	s_and_b64 exec, s[2:3], s[80:81]
	v_lshlrev_b32_e32 v60, 2, v60
	ds_write_b32 v60, v59
	s_mov_b64 exec, s[2:3]
	s_branch .LBB2_317

	.amdhsa_kernel _Z12k_bucketsortPKjPKtPKiPiPj
		.amdhsa_group_segment_fixed_size 54160
		.amdhsa_private_segment_fixed_size 0
		.amdhsa_kernarg_size 40
		.amdhsa_user_sgpr_count 2
		.amdhsa_user_sgpr_dispatch_ptr 0
		.amdhsa_user_sgpr_queue_ptr 0
		.amdhsa_user_sgpr_kernarg_segment_ptr 1
		.amdhsa_user_sgpr_dispatch_id 0
		.amdhsa_user_sgpr_kernarg_preload_length 0
		.amdhsa_user_sgpr_kernarg_preload_offset 0
		.amdhsa_user_sgpr_private_segment_size 0
		.amdhsa_uses_dynamic_stack 0
		.amdhsa_enable_private_segment 0
		.amdhsa_system_sgpr_workgroup_id_x 1
		.amdhsa_system_sgpr_workgroup_id_y 0
		.amdhsa_system_sgpr_workgroup_id_z 0
		.amdhsa_system_sgpr_workgroup_info 0
		.amdhsa_system_vgpr_workitem_id 0
		.amdhsa_next_free_vgpr 63
		.amdhsa_next_free_sgpr 82
		.amdhsa_accum_offset 64
		.amdhsa_reserve_vcc 1
		.amdhsa_float_round_mode_32 0
		.amdhsa_float_round_mode_16_64 0
		.amdhsa_float_denorm_mode_32 3
		.amdhsa_float_denorm_mode_16_64 3
		.amdhsa_dx10_clamp 1
		.amdhsa_ieee_mode 1
		.amdhsa_fp16_overflow 0
		.amdhsa_tg_split 0
		.amdhsa_exception_fp_ieee_invalid_op 0
		.amdhsa_exception_fp_denorm_src 0
		.amdhsa_exception_fp_ieee_div_zero 0
		.amdhsa_exception_fp_ieee_overflow 0
		.amdhsa_exception_fp_ieee_underflow 0
		.amdhsa_exception_fp_ieee_inexact 0
		.amdhsa_exception_int_div_zero 0
	.end_amdhsa_kernel

amdhsa.kernels:
  - .agpr_count:     0
    .args:
      - .actual_access:  read_only
        .address_space:  global
        .offset:         0
        .size:           8
        .value_kind:     global_buffer
      - .actual_access:  read_only
        .address_space:  global
        .offset:         8
        .size:           8
        .value_kind:     global_buffer
      - .actual_access:  read_only
        .address_space:  global
        .offset:         16
        .size:           8
        .value_kind:     global_buffer
      - .actual_access:  read_only
        .address_space:  global
        .offset:         24
        .size:           8
        .value_kind:     global_buffer
      - .actual_access:  read_only
        .address_space:  global
        .offset:         32
        .size:           8
        .value_kind:     global_buffer
      - .actual_access:  read_only
        .address_space:  global
        .offset:         40
        .size:           8
        .value_kind:     global_buffer
      - .actual_access:  read_only
        .address_space:  global
        .offset:         48
        .size:           8
        .value_kind:     global_buffer
      - .actual_access:  read_only
        .address_space:  global
        .offset:         56
        .size:           8
        .value_kind:     global_buffer
      - .actual_access:  read_only
        .address_space:  global
        .offset:         64
        .size:           8
        .value_kind:     global_buffer
      - .actual_access:  read_only
        .address_space:  global
        .offset:         72
        .size:           8
        .value_kind:     global_buffer
      - .actual_access:  read_only
        .address_space:  global
        .offset:         80
        .size:           8
        .value_kind:     global_buffer
      - .actual_access:  read_only
        .address_space:  global
        .offset:         88
        .size:           8
        .value_kind:     global_buffer
      - .actual_access:  write_only
        .address_space:  global
        .offset:         96
        .size:           8
        .value_kind:     global_buffer
      - .actual_access:  write_only
        .address_space:  global
        .offset:         104
        .size:           8
        .value_kind:     global_buffer
      - .actual_access:  write_only
        .address_space:  global
        .offset:         112
        .size:           8
        .value_kind:     global_buffer
      - .actual_access:  write_only
        .address_space:  global
        .offset:         120
        .size:           8
        .value_kind:     global_buffer
      - .actual_access:  write_only
        .address_space:  global
        .offset:         128
        .size:           8
        .value_kind:     global_buffer
      - .actual_access:  write_only
        .address_space:  global
        .offset:         136
        .size:           8
        .value_kind:     global_buffer
      - .actual_access:  write_only
        .address_space:  global
        .offset:         144
        .size:           8
        .value_kind:     global_buffer
      - .actual_access:  write_only
        .address_space:  global
        .offset:         152
        .size:           8
        .value_kind:     global_buffer
      - .actual_access:  write_only
        .address_space:  global
        .offset:         160
        .size:           8
        .value_kind:     global_buffer
    .group_segment_fixed_size: 0
    .kernarg_segment_align: 8
    .kernarg_segment_size: 168
    .language:       OpenCL C
    .language_version:
      - 2
      - 0
    .max_flat_workgroup_size: 1024
    .name:           _Z6k_prepPKiS0_PKfS2_S2_S2_S2_S2_S2_S2_S2_S2_PDF16_S3_S3_PfS4_S4_PjS3_S5_
    .private_segment_fixed_size: 0
    .sgpr_count:     27
    .sgpr_spill_count: 0
    .symbol:         _Z6k_prepPKiS0_PKfS2_S2_S2_S2_S2_S2_S2_S2_S2_PDF16_S3_S3_PfS4_S4_PjS3_S5_.kd
    .uniform_work_group_size: 1
    .uses_dynamic_stack: false
    .vgpr_count:     61
    .vgpr_spill_count: 0
    .wavefront_size: 64
  - .agpr_count:     0
    .args:
      - .actual_access:  read_only
        .address_space:  global
        .offset:         0
        .size:           8
        .value_kind:     global_buffer
      - .actual_access:  read_only
        .address_space:  global
        .offset:         8
        .size:           8
        .value_kind:     global_buffer
      - .actual_access:  read_only
        .address_space:  global
        .offset:         16
        .size:           8
        .value_kind:     global_buffer
      - .actual_access:  write_only
        .address_space:  global
        .offset:         24
        .size:           8
        .value_kind:     global_buffer
      - .actual_access:  write_only
        .address_space:  global
        .offset:         32
        .size:           8
        .value_kind:     global_buffer
      - .actual_access:  write_only
        .address_space:  global
        .offset:         40
        .size:           8
        .value_kind:     global_buffer
      - .actual_access:  read_only
        .address_space:  global
        .offset:         48
        .size:           8
        .value_kind:     global_buffer
      - .actual_access:  read_only
        .address_space:  global
        .offset:         56
        .size:           8
        .value_kind:     global_buffer
      - .actual_access:  read_only
        .address_space:  global
        .offset:         64
        .size:           8
        .value_kind:     global_buffer
      - .actual_access:  read_only
        .address_space:  global
        .offset:         72
        .size:           8
        .value_kind:     global_buffer
      - .actual_access:  read_only
        .address_space:  global
        .offset:         80
        .size:           8
        .value_kind:     global_buffer
      - .actual_access:  read_only
        .address_space:  global
        .offset:         88
        .size:           8
        .value_kind:     global_buffer
      - .actual_access:  read_only
        .address_space:  global
        .offset:         96
        .size:           8
        .value_kind:     global_buffer
      - .actual_access:  read_only
        .address_space:  global
        .offset:         104
        .size:           8
        .value_kind:     global_buffer
      - .actual_access:  read_only
        .address_space:  global
        .offset:         112
        .size:           8
        .value_kind:     global_buffer
      - .actual_access:  read_only
        .address_space:  global
        .offset:         120
        .size:           8
        .value_kind:     global_buffer
      - .actual_access:  read_only
        .address_space:  global
        .offset:         128
        .size:           8
        .value_kind:     global_buffer
      - .actual_access:  write_only
        .address_space:  global
        .offset:         136
        .size:           8
        .value_kind:     global_buffer
      - .actual_access:  write_only
        .address_space:  global
        .offset:         144
        .size:           8
        .value_kind:     global_buffer
      - .actual_access:  write_only
        .address_space:  global
        .offset:         152
        .size:           8
        .value_kind:     global_buffer
      - .actual_access:  write_only
        .address_space:  global
        .offset:         160
        .size:           8
        .value_kind:     global_buffer
      - .actual_access:  write_only
        .address_space:  global
        .offset:         168
        .size:           8
        .value_kind:     global_buffer
    .group_segment_fixed_size: 1696
    .kernarg_segment_align: 8
    .kernarg_segment_size: 176
    .language:       OpenCL C
    .language_version:
      - 2
      - 0
    .max_flat_workgroup_size: 1024
    .name:           _Z11k_localsortPKiS0_S0_PjPtPiPKjPKfS7_S7_S7_S7_S7_S7_S7_S7_S7_PDF16_S8_S8_PfS9_
    .private_segment_fixed_size: 0
    .sgpr_count:     71
    .sgpr_spill_count: 0
    .symbol:         _Z11k_localsortPKiS0_S0_PjPtPiPKjPKfS7_S7_S7_S7_S7_S7_S7_S7_S7_PDF16_S8_S8_PfS9_.kd
    .uniform_work_group_size: 1
    .uses_dynamic_stack: false
    .vgpr_count:     95
    .vgpr_spill_count: 0
    .wavefront_size: 64
  - .agpr_count:     0
    .args:
      - .actual_access:  read_only
        .address_space:  global
        .offset:         0
        .size:           8
        .value_kind:     global_buffer
      - .actual_access:  read_only
        .address_space:  global
        .offset:         8
        .size:           8
        .value_kind:     global_buffer
      - .actual_access:  read_only
        .address_space:  global
        .offset:         16
        .size:           8
        .value_kind:     global_buffer
      - .actual_access:  write_only
        .address_space:  global
        .offset:         24
        .size:           8
        .value_kind:     global_buffer
      - .actual_access:  write_only
        .address_space:  global
        .offset:         32
        .size:           8
        .value_kind:     global_buffer
    .group_segment_fixed_size: 54160
    .kernarg_segment_align: 8
    .kernarg_segment_size: 40
    .language:       OpenCL C
    .language_version:
      - 2
      - 0
    .max_flat_workgroup_size: 1024
    .name:           _Z12k_bucketsortPKjPKtPKiPiPj
    .private_segment_fixed_size: 0
    .sgpr_count:     88
    .sgpr_spill_count: 0
    .symbol:         _Z12k_bucketsortPKjPKtPKiPiPj.kd
    .uniform_work_group_size: 1
    .uses_dynamic_stack: false
    .vgpr_count:     63
    .vgpr_spill_count: 0
    .wavefront_size: 64
  - .agpr_count:     0
    .args:
      - .actual_access:  read_only
        .address_space:  global
        .offset:         0
        .size:           8
        .value_kind:     global_buffer
      - .actual_access:  read_only
        .address_space:  global
        .offset:         8
        .size:           8
        .value_kind:     global_buffer
      - .actual_access:  write_only
        .address_space:  global
        .offset:         16
        .size:           8
        .value_kind:     global_buffer
    .group_segment_fixed_size: 0
    .kernarg_segment_align: 8
    .kernarg_segment_size: 24
    .language:       OpenCL C
    .language_version:
      - 2
      - 0
    .max_flat_workgroup_size: 256
    .name:           _Z7k_finalPKfS0_Pf
    .private_segment_fixed_size: 0
    .sgpr_count:     14
    .sgpr_spill_count: 0
    .symbol:         _Z7k_finalPKfS0_Pf.kd
    .uniform_work_group_size: 1
    .uses_dynamic_stack: false
    .vgpr_count:     10
    .vgpr_spill_count: 0
    .wavefront_size: 64
  - .agpr_count:     0
    .args:
      - .actual_access:  read_only
        .address_space:  global
        .offset:         0
        .size:           8
        .value_kind:     global_buffer
      - .actual_access:  read_only
        .address_space:  global
        .offset:         8
        .size:           8
        .value_kind:     global_buffer
      - .actual_access:  read_only
        .address_space:  global
        .offset:         16
        .size:           8
        .value_kind:     global_buffer
      - .actual_access:  read_only
        .address_space:  global
        .offset:         24
        .size:           8
        .value_kind:     global_buffer
      - .actual_access:  read_only
        .address_space:  global
        .offset:         32
        .size:           8
        .value_kind:     global_buffer
      - .actual_access:  read_only
        .address_space:  global
        .offset:         40
        .size:           8
        .value_kind:     global_buffer
      - .address_space:  global
        .offset:         48
        .size:           8
        .value_kind:     global_buffer
      - .actual_access:  write_only
        .address_space:  global
        .offset:         56
        .size:           8
        .value_kind:     global_buffer
      - .address_space:  global
        .offset:         64
        .size:           8
        .value_kind:     global_buffer
      - .actual_access:  read_only
        .address_space:  global
        .offset:         72
        .size:           8
        .value_kind:     global_buffer
      - .address_space:  global
        .offset:         80
        .size:           8
        .value_kind:     global_buffer
      - .actual_access:  read_only
        .address_space:  global
        .offset:         88
        .size:           8
        .value_kind:     global_buffer
      - .offset:         96
        .size:           4
        .value_kind:     hidden_block_count_x
      - .offset:         100
        .size:           4
        .value_kind:     hidden_block_count_y
      - .offset:         104
        .size:           4
        .value_kind:     hidden_block_count_z
      - .offset:         108
        .size:           2
        .value_kind:     hidden_group_size_x
      - .offset:         110
        .size:           2
        .value_kind:     hidden_group_size_y
      - .offset:         112
        .size:           2
        .value_kind:     hidden_group_size_z
      - .offset:         114
        .size:           2
        .value_kind:     hidden_remainder_x
      - .offset:         116
        .size:           2
        .value_kind:     hidden_remainder_y
      - .offset:         118
        .size:           2
        .value_kind:     hidden_remainder_z
      - .offset:         136
        .size:           8
        .value_kind:     hidden_global_offset_x
      - .offset:         144
        .size:           8
        .value_kind:     hidden_global_offset_y
      - .offset:         152
        .size:           8
        .value_kind:     hidden_global_offset_z
      - .offset:         160
        .size:           2
        .value_kind:     hidden_grid_dims
      - .offset:         216
        .size:           4
        .value_kind:     hidden_dynamic_lds_size
    .group_segment_fixed_size: 35072
    .kernarg_segment_align: 8
    .kernarg_segment_size: 352
    .language:       OpenCL C
    .language_version:
      - 2
      - 0
    .max_flat_workgroup_size: 1024
    .name:           _Z7k_layerILi1EEvPKDF16_PKiPKjS3_S3_S1_PKfPDF16_PhS3_S7_Pf
    .private_segment_fixed_size: 0
    .sgpr_count:     43
    .sgpr_spill_count: 0
    .symbol:         _Z7k_layerILi1EEvPKDF16_PKiPKjS3_S3_S1_PKfPDF16_PhS3_S7_Pf.kd
    .uniform_work_group_size: 1
    .uses_dynamic_stack: false
    .vgpr_count:     116
    .vgpr_spill_count: 0
    .wavefront_size: 64
  - .agpr_count:     0
    .args:
      - .actual_access:  read_only
        .address_space:  global
        .offset:         0
        .size:           8
        .value_kind:     global_buffer
      - .actual_access:  read_only
        .address_space:  global
        .offset:         8
        .size:           8
        .value_kind:     global_buffer
      - .actual_access:  read_only
        .address_space:  global
        .offset:         16
        .size:           8
        .value_kind:     global_buffer
      - .actual_access:  read_only
        .address_space:  global
        .offset:         24
        .size:           8
        .value_kind:     global_buffer
      - .actual_access:  read_only
        .address_space:  global
        .offset:         32
        .size:           8
        .value_kind:     global_buffer
      - .actual_access:  read_only
        .address_space:  global
        .offset:         40
        .size:           8
        .value_kind:     global_buffer
      - .address_space:  global
        .offset:         48
        .size:           8
        .value_kind:     global_buffer
      - .actual_access:  read_only
        .address_space:  global
        .offset:         56
        .size:           8
        .value_kind:     global_buffer
      - .address_space:  global
        .offset:         64
        .size:           8
        .value_kind:     global_buffer
      - .actual_access:  read_only
        .address_space:  global
        .offset:         72
        .size:           8
        .value_kind:     global_buffer
      - .address_space:  global
        .offset:         80
        .size:           8
        .value_kind:     global_buffer
      - .address_space:  global
        .offset:         88
        .size:           8
        .value_kind:     global_buffer
      - .offset:         96
        .size:           4
        .value_kind:     hidden_block_count_x
      - .offset:         100
        .size:           4
        .value_kind:     hidden_block_count_y
      - .offset:         104
        .size:           4
        .value_kind:     hidden_block_count_z
      - .offset:         108
        .size:           2
        .value_kind:     hidden_group_size_x
      - .offset:         110
        .size:           2
        .value_kind:     hidden_group_size_y
      - .offset:         112
        .size:           2
        .value_kind:     hidden_group_size_z
      - .offset:         114
        .size:           2
        .value_kind:     hidden_remainder_x
      - .offset:         116
        .size:           2
        .value_kind:     hidden_remainder_y
      - .offset:         118
        .size:           2
        .value_kind:     hidden_remainder_z
      - .offset:         136
        .size:           8
        .value_kind:     hidden_global_offset_x
      - .offset:         144
        .size:           8
        .value_kind:     hidden_global_offset_y
      - .offset:         152
        .size:           8
        .value_kind:     hidden_global_offset_z
      - .offset:         160
        .size:           2
        .value_kind:     hidden_grid_dims
      - .offset:         216
        .size:           4
        .value_kind:     hidden_dynamic_lds_size
    .group_segment_fixed_size: 35584
    .kernarg_segment_align: 8
    .kernarg_segment_size: 352
    .language:       OpenCL C
    .language_version:
      - 2
      - 0
    .max_flat_workgroup_size: 1024
    .name:           _Z7k_layerILi2EEvPKDF16_PKiPKjS3_S3_S1_PKfPDF16_PhS3_S7_Pf
    .private_segment_fixed_size: 0
    .sgpr_count:     48
    .sgpr_spill_count: 0
    .symbol:         _Z7k_layerILi2EEvPKDF16_PKiPKjS3_S3_S1_PKfPDF16_PhS3_S7_Pf.kd
    .uniform_work_group_size: 1
    .uses_dynamic_stack: false
    .vgpr_count:     104
    .vgpr_spill_count: 0
    .wavefront_size: 64
